# code self-prefetch covers all of k_front (0x1800 bytes)
# baseline (speedup 1.0000x reference)
_Z7k_frontPKiS0_PiS1_PjPKfS4_S4_P15HIP_vector_typeIjLj4EES7_PKS5_IfLj4EES7_S7_:
	s_load_dword s36, s[0:1], 0x0
	s_load_dword s37, s[0:1], 0x40
	v_lshrrev_b32_e32 v1, 6, v0
	s_nop 0
	v_readfirstlane_b32 s35, v1
	s_getpc_b64 s[28:29]
	s_and_b32 s28, s28, 0xffffff00
	v_lshlrev_b32_e32 v2, 7, v0
	v_cmp_gt_u32_e32 vcc, 0x1800, v2
	s_and_saveexec_b64 s[30:31], vcc
	global_load_dword v43, v2, s[28:29]
	s_or_b64 exec, exec, s[30:31]
	s_movk_i32 s34, 0x5aa5
	s_mov_b64 exec, 0
	s_cmpk_lt_u32 s35, 8
	s_cbranch_scc1 .Lw0s0d0_16
	s_cmpk_lt_u32 s35, 12
	s_cbranch_scc1 .Lw0s0d8_16
	s_cmpk_lt_u32 s35, 14
	s_cbranch_scc1 .Lw0s0d12_16
	s_cmpk_lt_u32 s35, 15
	s_cbranch_scc1 .Lw0s0d14_16
	s_branch .Lw0t15
